# GU L1 K-loop: longer LDS-DMA lead (trailing half issues next-phase DMA groups at the head of its MFMA block; leading half waits after its MFMA block)
# baseline (speedup 1.0000x reference)
; #define PG8_STAGE(bufoff, gbase, voff) do { _Pragma("unroll") for (int _i = 0; _i < 2; ++_i) \
;         __builtin_amdgcn_global_load_lds((const unsigned*)((const char*)(gbase) + (voff)[_i]), (LAS unsigned*)(lds + (bufoff) + ldsw + _i * 8192), 16, 0, 0); } while (0)
; #define PG8_LDA(dst, b, h) do { _Pragma("unroll") for (int m = 0; m < 4; ++m) _Pragma("unroll") for (int k = 0; k < 2; ++k) dst[m][k] = *(const LAS bf16x8*)(lds + PG8_SA(b, h) + ((aoff ^ (k * 64)) + m * 2048)); } while (0)
; #define PG8_LDB(dst, b, h) do { _Pragma("unroll") for (int n = 0; n < 2; ++n) _Pragma("unroll") for (int k = 0; k < 2; ++k) dst[n][k] = *(const LAS bf16x8*)(lds + PG8_SB(b, h) + ((boff ^ (k * 64)) + n * 2048)); } while (0)
; #define PG8_BAR __builtin_amdgcn_s_barrier()
;     ...
;             const bool last = (t == nt - 2);
;             const char* a1 = cA + (size_t)(t + 1) * kstepA;
;             const char* a2 = last ? nA : cA + (size_t)(t + 2) * kstepA; const char* b2 = last ? nB : cB + (size_t)(t + 2) * kstepB;
;             const char* a3 = a2 + kstepA; const char* b3 = b2 + kstepB;
;             unsigned vs[2][2];
;             if constexpr (GATHER) {
;                 if (last && has_next) {
; #pragma unroll
;                     for (int hh = 0; hh < 2; ++hh)
; #pragma unroll
;                         for (int i = 0; i < 2; ++i) voffN[hh][i] = (unsigned)idxl[(ui + 1) * 256 + hh * HALF + sR[i]] * (unsigned)(K * 2) + (unsigned)sC[i] * 2u;
;                 }
; #pragma unroll
;                 for (int hh = 0; hh < 2; ++hh)
; #pragma unroll
;                     for (int i = 0; i < 2; ++i) vs[hh][i] = last ? voffN[hh][i] : voffA[hh][i];
;             } else {
; #pragma unroll
;                 for (int hh = 0; hh < 2; ++hh)
; #pragma unroll
;                     for (int i = 0; i < 2; ++i) vs[hh][i] = voffA[hh][i];
;             }
;             PG8_LDB(B0, 0, 0); PG8_LDB(B1, 0, 1); PG8_SCHED; PG8_LDA(At, 0, 0); PG8_STAGE(PG8_SA(1, 1), a1, voffA[1]);
;             PG8_WAIT_V(8); PG8_WAIT_L(0); PG8_BAR; if (do0) { PG8_MMA(0, 0, At, B0); PG8_MMA(0, 1, At, B1); } PG8_BAR; PG8_SCHED;
;             PG8_LDA(At, 0, 1); PG8_STAGE(PG8_SB(0, 0), b2, voffB); PG8_STAGE(PG8_SB(0, 1), b2 + hstep, voffB); PG8_STAGE(PG8_SA(0, 0), a2, vs[0]);
;             PG8_WAIT_V(8); PG8_WAIT_L(0); PG8_BAR; if (do1) { PG8_MMA(1, 0, At, B0); PG8_MMA(1, 1, At, B1); } PG8_BAR; PG8_SCHED;
.LBB0_2337:
	v_add_u32_e32 v136, s43, v159
	v_add_u32_e32 v145, s43, v160
	ds_read_b128 v[166:169], v136
	ds_read_b128 v[170:173], v145
	v_add_u32_e32 v136, s44, v159
	s_add_u32 s22, s90, s20
	v_add_u32_e32 v145, s44, v160
	ds_read_b128 v[174:177], v136
	ds_read_b128 v[178:181], v145
	v_add_u32_e32 v136, s45, v159
	s_addc_u32 s23, s91, s21
	v_add_u32_e32 v145, s45, v160
	ds_read_b128 v[182:185], v136
	ds_read_b128 v[186:189], v145
	v_add_u32_e32 v136, s46, v159
	s_add_u32 s24, s22, 0x4213700
	v_add_u32_e32 v145, s46, v160
	ds_read_b128 v[190:193], v136
	ds_read_b128 v[194:197], v145
	s_addc_u32 s25, s23, 0
	s_and_b64 s[22:23], s[2:3], exec
	s_cselect_b32 s22, s14, s13
	s_cselect_b32 s27, s83, s25
	s_cselect_b32 s26, s82, s24
	s_cselect_b32 s23, s15, s53
	s_add_u32 s24, s22, 0x4000
	s_addc_u32 s25, s23, 0
	v_cndmask_b32_e64 v136, v152, v146, s[2:3]
	v_cndmask_b32_e64 v232, v153, v147, s[2:3]
	v_cndmask_b32_e64 v145, v148, v164, s[2:3]
	v_cndmask_b32_e64 v149, v150, v165, s[2:3]
	ds_read_b128 v[200:203], v161
	ds_read_b128 v[204:207], v161 offset:2048
	ds_read_b128 v[208:211], v162
	ds_read_b128 v[212:215], v162 offset:2048
	ds_read_b128 v[216:219], v161 offset:4096
	ds_read_b128 v[220:223], v161 offset:6144
	ds_read_b128 v[224:227], v162 offset:4096
	ds_read_b128 v[228:231], v162 offset:6144
	v_lshl_add_u64 v[234:235], v[156:157], 0, s[20:21]
	s_add_i32 m0, s17, 0xc000
	s_nop 0
	global_load_lds_dwordx4 v[234:235], off
	v_lshl_add_u64 v[234:235], v[154:155], 0, s[20:21]
	s_add_i32 m0, s17, 0xe000
	s_nop 0
	global_load_lds_dwordx4 v[234:235], off
	s_bitcmp1_b32 s4, 0
	s_cbranch_scc0 .Lld_gu1_sp1a_j
	s_waitcnt vmcnt(8)
.Lld_gu1_sp1a_j:
	s_waitcnt lgkmcnt(0)
	s_barrier
	s_bitcmp1_b32 s4, 0
	s_cbranch_scc0 .Lld_gu1_m1a_m
	s_add_i32 s2, s43, s34
	v_lshl_add_u64 v[234:235], s[22:23], 0, v[132:133]
	s_mov_b32 m0, s2
	s_nop 0
	global_load_lds_dwordx4 v[234:235], off
	s_add_i32 m0, s2, 0x2000
	s_add_u32 s2, s22, 0x40000
	v_lshl_add_u64 v[234:235], s[22:23], 0, v[134:135]
	s_addc_u32 s3, s23, 0
	s_add_i32 s55, s45, s34
	global_load_lds_dwordx4 v[234:235], off
	v_lshl_add_u64 v[234:235], s[2:3], 0, v[132:133]
	s_mov_b32 m0, s55
	v_mov_b32_e32 v233, v137
	global_load_lds_dwordx4 v[234:235], off
	v_lshl_add_u64 v[234:235], s[2:3], 0, v[134:135]
	s_add_i32 m0, s55, 0x2000
	s_nop 0
	global_load_lds_dwordx4 v[234:235], off
	s_mov_b32 m0, s17
	v_lshl_add_u64 v[234:235], s[26:27], 0, v[136:137]
	global_load_lds_dwordx4 v136, s[26:27]
	s_mov_b32 m0, s35
	s_nop 0
	global_load_lds_dwordx4 v232, s[26:27]
	v_lshl_add_u64 v[232:233], s[26:27], 0, v[232:233]
.Lld_gu1_m1a_m:
	s_setprio 1
	s_waitcnt lgkmcnt(0)
	v_mfma_f32_16x16x32_bf16 v[126:129], v[166:169], v[200:203], v[126:129]
	v_mfma_f32_16x16x32_bf16 v[122:125], v[174:177], v[200:203], v[122:125]
	v_mfma_f32_16x16x32_bf16 v[110:113], v[166:169], v[204:207], v[110:113]
	v_mfma_f32_16x16x32_bf16 v[106:109], v[174:177], v[204:207], v[106:109]
	v_mfma_f32_16x16x32_bf16 v[94:97], v[166:169], v[216:219], v[94:97]
	v_mfma_f32_16x16x32_bf16 v[90:93], v[174:177], v[216:219], v[90:93]
	v_mfma_f32_16x16x32_bf16 v[78:81], v[166:169], v[220:223], v[78:81]
	v_mfma_f32_16x16x32_bf16 v[74:77], v[174:177], v[220:223], v[74:77]
	v_mfma_f32_16x16x32_bf16 v[126:129], v[170:173], v[208:211], v[126:129]
	v_mfma_f32_16x16x32_bf16 v[122:125], v[178:181], v[208:211], v[122:125]
	v_mfma_f32_16x16x32_bf16 v[110:113], v[170:173], v[212:215], v[110:113]
	v_mfma_f32_16x16x32_bf16 v[106:109], v[178:181], v[212:215], v[106:109]
	v_mfma_f32_16x16x32_bf16 v[94:97], v[170:173], v[224:227], v[94:97]
	v_mfma_f32_16x16x32_bf16 v[90:93], v[178:181], v[224:227], v[90:93]
	v_mfma_f32_16x16x32_bf16 v[78:81], v[170:173], v[228:231], v[78:81]
	v_mfma_f32_16x16x32_bf16 v[74:77], v[178:181], v[228:231], v[74:77]
	s_setprio 0
	s_setprio 1
	v_mfma_f32_16x16x32_bf16 v[118:121], v[182:185], v[200:203], v[118:121]
	v_mfma_f32_16x16x32_bf16 v[114:117], v[190:193], v[200:203], v[114:117]
	v_mfma_f32_16x16x32_bf16 v[102:105], v[182:185], v[204:207], v[102:105]
	v_mfma_f32_16x16x32_bf16 v[98:101], v[190:193], v[204:207], v[98:101]
	v_mfma_f32_16x16x32_bf16 v[86:89], v[182:185], v[216:219], v[86:89]
	v_mfma_f32_16x16x32_bf16 v[82:85], v[190:193], v[216:219], v[82:85]
	v_mfma_f32_16x16x32_bf16 v[70:73], v[182:185], v[220:223], v[70:73]
	v_mfma_f32_16x16x32_bf16 v[66:69], v[190:193], v[220:223], v[66:69]
	v_mfma_f32_16x16x32_bf16 v[118:121], v[186:189], v[208:211], v[118:121]
	v_mfma_f32_16x16x32_bf16 v[114:117], v[194:197], v[208:211], v[114:117]
	v_mfma_f32_16x16x32_bf16 v[102:105], v[186:189], v[212:215], v[102:105]
	v_mfma_f32_16x16x32_bf16 v[98:101], v[194:197], v[212:215], v[98:101]
	v_mfma_f32_16x16x32_bf16 v[86:89], v[186:189], v[224:227], v[86:89]
	v_mfma_f32_16x16x32_bf16 v[82:85], v[194:197], v[224:227], v[82:85]
	v_mfma_f32_16x16x32_bf16 v[70:73], v[186:189], v[228:231], v[70:73]
	v_mfma_f32_16x16x32_bf16 v[66:69], v[194:197], v[228:231], v[66:69]
	s_setprio 0
	s_bitcmp1_b32 s4, 0
	s_cbranch_scc1 .Lld_gu1_m1a_p
	s_waitcnt vmcnt(8)
; #define PG8_STAGE(bufoff, gbase, voff) do { _Pragma("unroll") for (int _i = 0; _i < 2; ++_i) \
;         __builtin_amdgcn_global_load_lds((const unsigned*)((const char*)(gbase) + (voff)[_i]), (LAS unsigned*)(lds + (bufoff) + ldsw + _i * 8192), 16, 0, 0); } while (0)
; #define PG8_LDA(dst, b, h) do { _Pragma("unroll") for (int m = 0; m < 4; ++m) _Pragma("unroll") for (int k = 0; k < 2; ++k) dst[m][k] = *(const LAS bf16x8*)(lds + PG8_SA(b, h) + ((aoff ^ (k * 64)) + m * 2048)); } while (0)
; #define PG8_LDB(dst, b, h) do { _Pragma("unroll") for (int n = 0; n < 2; ++n) _Pragma("unroll") for (int k = 0; k < 2; ++k) dst[n][k] = *(const LAS bf16x8*)(lds + PG8_SB(b, h) + ((boff ^ (k * 64)) + n * 2048)); } while (0)
; #define PG8_MMA(ai, bj, At, Bt) do { __builtin_amdgcn_s_setprio(1); _Pragma("unroll") for (int m = 0; m < 4; ++m) _Pragma("unroll") for (int n = 0; n < 2; ++n) _Pragma("unroll") for (int k = 0; k < 2; ++k) \
;         acc[ai][bj][m][n] = __builtin_amdgcn_mfma_f32_16x16x32_bf16(Bt[n][k], At[m][k], acc[ai][bj][m][n], 0, 0, 0); __builtin_amdgcn_s_setprio(0); } while (0)
; #define PG8_WAIT_V(n) asm volatile("s_waitcnt vmcnt(" #n ")" ::: "memory")
; #define PG8_WAIT_L(n) asm volatile("s_waitcnt lgkmcnt(" #n ")" ::: "memory")
; #define PG8_BAR __builtin_amdgcn_s_barrier()
; #define PG8_SCHED __builtin_amdgcn_sched_barrier(0)
;     ...
;             PG8_LDA(At, 0, 1); PG8_STAGE(PG8_SB(0, 0), b2, voffB); PG8_STAGE(PG8_SB(0, 1), b2 + hstep, voffB); PG8_STAGE(PG8_SA(0, 0), a2, vs[0]);
;             PG8_WAIT_V(8); PG8_WAIT_L(0); PG8_BAR; if (do1) { PG8_MMA(1, 0, At, B0); PG8_MMA(1, 1, At, B1); } PG8_BAR; PG8_SCHED;
;             PG8_LDB(B0, 1, 0); PG8_LDB(B1, 1, 1); PG8_SCHED; PG8_LDA(At, 1, 0); PG8_STAGE(PG8_SA(0, 1), a2, vs[1]);
;             PG8_WAIT_V(8); PG8_WAIT_L(0); PG8_BAR; if (do0) { PG8_MMA(0, 0, At, B0); PG8_MMA(0, 1, At, B1); } PG8_BAR; PG8_SCHED;
.Lld_gu1_m1a_p:
	s_barrier
	ds_read_b128 v[200:203], v161 offset:16384
	ds_read_b128 v[204:207], v161 offset:18432
	ds_read_b128 v[208:211], v162 offset:16384
	ds_read_b128 v[212:215], v162 offset:18432
	ds_read_b128 v[216:219], v161 offset:20480
	ds_read_b128 v[220:223], v161 offset:22528
	ds_read_b128 v[224:227], v162 offset:20480
	ds_read_b128 v[228:231], v162 offset:22528
	s_bitcmp1_b32 s4, 0
	s_cbranch_scc1 .Lld_gu1_sp2a_w
	s_add_i32 s2, s43, s34
	v_lshl_add_u64 v[234:235], s[22:23], 0, v[132:133]
	s_mov_b32 m0, s2
	s_nop 0
	global_load_lds_dwordx4 v[234:235], off
	s_add_i32 m0, s2, 0x2000
	s_add_u32 s2, s22, 0x40000
	v_lshl_add_u64 v[234:235], s[22:23], 0, v[134:135]
	s_addc_u32 s3, s23, 0
	s_add_i32 s55, s45, s34
	global_load_lds_dwordx4 v[234:235], off
	v_lshl_add_u64 v[234:235], s[2:3], 0, v[132:133]
	s_mov_b32 m0, s55
	v_mov_b32_e32 v233, v137
	global_load_lds_dwordx4 v[234:235], off
	v_lshl_add_u64 v[234:235], s[2:3], 0, v[134:135]
	s_add_i32 m0, s55, 0x2000
	s_nop 0
	global_load_lds_dwordx4 v[234:235], off
	s_mov_b32 m0, s17
	v_lshl_add_u64 v[234:235], s[26:27], 0, v[136:137]
	global_load_lds_dwordx4 v136, s[26:27]
	s_mov_b32 m0, s35
	s_nop 0
	global_load_lds_dwordx4 v232, s[26:27]
	v_lshl_add_u64 v[232:233], s[26:27], 0, v[232:233]
	s_branch .Lld_gu1_sp2a_j
.Lld_gu1_sp2a_w:
	s_waitcnt vmcnt(8)
.Lld_gu1_sp2a_j:
	s_waitcnt lgkmcnt(0)
	s_barrier
	s_bitcmp1_b32 s4, 0
	s_cbranch_scc0 .Lld_gu1_m2a_m
	s_mov_b32 m0, s36
	s_nop 0
	global_load_lds_dwordx4 v145, s[26:27]
	s_mov_b32 m0, s37
	s_nop 0
	global_load_lds_dwordx4 v149, s[26:27]
.Lld_gu1_m2a_m:
	s_setprio 1
	s_waitcnt lgkmcnt(0)
	v_mfma_f32_16x16x32_bf16 v[62:65], v[166:169], v[200:203], v[62:65]
	v_mfma_f32_16x16x32_bf16 v[58:61], v[174:177], v[200:203], v[58:61]
	v_mfma_f32_16x16x32_bf16 v[46:49], v[166:169], v[204:207], v[46:49]
	v_mfma_f32_16x16x32_bf16 v[42:45], v[174:177], v[204:207], v[42:45]
	v_mfma_f32_16x16x32_bf16 v[30:33], v[166:169], v[216:219], v[30:33]
	v_mfma_f32_16x16x32_bf16 v[26:29], v[174:177], v[216:219], v[26:29]
	v_mfma_f32_16x16x32_bf16 v[14:17], v[166:169], v[220:223], v[14:17]
	v_mfma_f32_16x16x32_bf16 v[10:13], v[174:177], v[220:223], v[10:13]
	v_mfma_f32_16x16x32_bf16 v[62:65], v[170:173], v[208:211], v[62:65]
	v_mfma_f32_16x16x32_bf16 v[58:61], v[178:181], v[208:211], v[58:61]
	v_mfma_f32_16x16x32_bf16 v[46:49], v[170:173], v[212:215], v[46:49]
	v_mfma_f32_16x16x32_bf16 v[42:45], v[178:181], v[212:215], v[42:45]
	v_mfma_f32_16x16x32_bf16 v[30:33], v[170:173], v[224:227], v[30:33]
	v_mfma_f32_16x16x32_bf16 v[26:29], v[178:181], v[224:227], v[26:29]
	v_mfma_f32_16x16x32_bf16 v[14:17], v[170:173], v[228:231], v[14:17]
	v_mfma_f32_16x16x32_bf16 v[10:13], v[178:181], v[228:231], v[10:13]
	s_setprio 0
	s_setprio 1
	v_mfma_f32_16x16x32_bf16 v[54:57], v[182:185], v[200:203], v[54:57]
	v_mfma_f32_16x16x32_bf16 v[50:53], v[190:193], v[200:203], v[50:53]
	v_mfma_f32_16x16x32_bf16 v[38:41], v[182:185], v[204:207], v[38:41]
	v_mfma_f32_16x16x32_bf16 v[34:37], v[190:193], v[204:207], v[34:37]
	v_mfma_f32_16x16x32_bf16 v[22:25], v[182:185], v[216:219], v[22:25]
	v_mfma_f32_16x16x32_bf16 v[18:21], v[190:193], v[216:219], v[18:21]
	v_mfma_f32_16x16x32_bf16 v[6:9], v[182:185], v[220:223], v[6:9]
	v_mfma_f32_16x16x32_bf16 v[2:5], v[190:193], v[220:223], v[2:5]
	v_mfma_f32_16x16x32_bf16 v[54:57], v[186:189], v[208:211], v[54:57]
	v_mfma_f32_16x16x32_bf16 v[50:53], v[194:197], v[208:211], v[50:53]
	v_mfma_f32_16x16x32_bf16 v[38:41], v[186:189], v[212:215], v[38:41]
	v_mfma_f32_16x16x32_bf16 v[34:37], v[194:197], v[212:215], v[34:37]
	v_mfma_f32_16x16x32_bf16 v[22:25], v[186:189], v[224:227], v[22:25]
	v_mfma_f32_16x16x32_bf16 v[18:21], v[194:197], v[224:227], v[18:21]
	v_mfma_f32_16x16x32_bf16 v[6:9], v[186:189], v[228:231], v[6:9]
	v_mfma_f32_16x16x32_bf16 v[2:5], v[194:197], v[228:231], v[2:5]
	s_setprio 0
	s_bitcmp1_b32 s4, 0
	s_cbranch_scc1 .Lld_gu1_m2a_p
	s_waitcnt vmcnt(8)
.Lld_gu1_m2a_p:
	s_barrier
	s_add_i32 s2, 0, 0x18000
	v_add_u32_e32 v136, s2, v159
	v_add_u32_e32 v151, s2, v160
	ds_read_b128 v[166:169], v136
	ds_read_b128 v[170:173], v151
	v_add_u32_e32 v136, s47, v159
	s_add_i32 s55, 0, 0x1c000
	v_add_u32_e32 v151, s47, v160
	ds_read_b128 v[174:177], v136
	ds_read_b128 v[178:181], v151
	v_add_u32_e32 v136, s55, v159
	v_add_u32_e32 v151, s55, v160
	ds_read_b128 v[182:185], v136
	ds_read_b128 v[186:189], v151
	v_add_u32_e32 v136, s48, v159
	v_add_u32_e32 v151, s48, v160
	ds_read_b128 v[190:193], v136
	ds_read_b128 v[194:197], v151
	ds_read_b128 v[200:203], v161 offset:32768
	ds_read_b128 v[204:207], v161 offset:34816
	ds_read_b128 v[208:211], v162 offset:32768
	ds_read_b128 v[212:215], v162 offset:34816
	ds_read_b128 v[216:219], v161 offset:36864
	ds_read_b128 v[220:223], v161 offset:38912
	ds_read_b128 v[224:227], v162 offset:36864
	ds_read_b128 v[228:231], v162 offset:38912
	s_bitcmp1_b32 s4, 0
	s_cbranch_scc1 .Lld_gu1_sp1b_w
	s_mov_b32 m0, s36
	s_nop 0
	global_load_lds_dwordx4 v145, s[26:27]
	s_mov_b32 m0, s37
	s_nop 0
	global_load_lds_dwordx4 v149, s[26:27]
	s_branch .Lld_gu1_sp1b_j

; #define PG8_STAGE(bufoff, gbase, voff) do { _Pragma("unroll") for (int _i = 0; _i < 2; ++_i) \
;         __builtin_amdgcn_global_load_lds((const unsigned*)((const char*)(gbase) + (voff)[_i]), (LAS unsigned*)(lds + (bufoff) + ldsw + _i * 8192), 16, 0, 0); } while (0)
; #define PG8_LDA(dst, b, h) do { _Pragma("unroll") for (int m = 0; m < 4; ++m) _Pragma("unroll") for (int k = 0; k < 2; ++k) dst[m][k] = *(const LAS bf16x8*)(lds + PG8_SA(b, h) + ((aoff ^ (k * 64)) + m * 2048)); } while (0)
; #define PG8_LDB(dst, b, h) do { _Pragma("unroll") for (int n = 0; n < 2; ++n) _Pragma("unroll") for (int k = 0; k < 2; ++k) dst[n][k] = *(const LAS bf16x8*)(lds + PG8_SB(b, h) + ((boff ^ (k * 64)) + n * 2048)); } while (0)
; #define PG8_MMA(ai, bj, At, Bt) do { __builtin_amdgcn_s_setprio(1); _Pragma("unroll") for (int m = 0; m < 4; ++m) _Pragma("unroll") for (int n = 0; n < 2; ++n) _Pragma("unroll") for (int k = 0; k < 2; ++k) \
;         acc[ai][bj][m][n] = __builtin_amdgcn_mfma_f32_16x16x32_bf16(Bt[n][k], At[m][k], acc[ai][bj][m][n], 0, 0, 0); __builtin_amdgcn_s_setprio(0); } while (0)
; #define PG8_WAIT_V(n) asm volatile("s_waitcnt vmcnt(" #n ")" ::: "memory")
; #define PG8_WAIT_L(n) asm volatile("s_waitcnt lgkmcnt(" #n ")" ::: "memory")
; #define PG8_BAR __builtin_amdgcn_s_barrier()
; #define PG8_SCHED __builtin_amdgcn_sched_barrier(0)
;     ...
;             PG8_LDB(B0, 1, 0); PG8_LDB(B1, 1, 1); PG8_SCHED; PG8_LDA(At, 1, 0); PG8_STAGE(PG8_SA(0, 1), a2, vs[1]);
;             PG8_WAIT_V(8); PG8_WAIT_L(0); PG8_BAR; if (do0) { PG8_MMA(0, 0, At, B0); PG8_MMA(0, 1, At, B1); } PG8_BAR; PG8_SCHED;
;             PG8_LDA(At, 1, 1); PG8_STAGE(PG8_SB(1, 0), b3, voffB); PG8_STAGE(PG8_SB(1, 1), b3 + hstep, voffB); PG8_STAGE(PG8_SA(1, 0), a3, vs[0]);
.Lld_gu1_sp1b_j:
	s_waitcnt lgkmcnt(0)
	s_barrier
	s_bitcmp1_b32 s4, 0
	s_cbranch_scc0 .Lld_gu1_m1b_m
	s_add_i32 s2, s2, s34
	v_lshl_add_u64 v[236:237], s[24:25], 0, v[132:133]
	s_mov_b32 m0, s2
	s_nop 0
	global_load_lds_dwordx4 v[236:237], off
	s_add_i32 m0, s2, 0x2000
	s_add_u32 s2, s22, 0x44000
	v_lshl_add_u64 v[236:237], s[24:25], 0, v[134:135]
	s_addc_u32 s3, s23, 0
	s_add_i32 s22, s55, s34
	global_load_lds_dwordx4 v[236:237], off
	v_lshl_add_u64 v[236:237], s[2:3], 0, v[132:133]
	s_mov_b32 m0, s22
	v_lshl_add_u64 v[234:235], v[234:235], 0, s[10:11]
	global_load_lds_dwordx4 v[236:237], off
	v_lshl_add_u64 v[236:237], s[2:3], 0, v[134:135]
	s_add_i32 m0, s22, 0x2000
	v_lshl_add_u64 v[232:233], v[232:233], 0, s[10:11]
	global_load_lds_dwordx4 v[236:237], off
	s_mov_b32 m0, s41
	s_nop 0
	global_load_lds_dwordx4 v[234:235], off
	s_mov_b32 m0, s42
	s_nop 0
	global_load_lds_dwordx4 v[232:233], off

; #define PG8_STAGE(bufoff, gbase, voff) do { _Pragma("unroll") for (int _i = 0; _i < 2; ++_i) \
;         __builtin_amdgcn_global_load_lds((const unsigned*)((const char*)(gbase) + (voff)[_i]), (LAS unsigned*)(lds + (bufoff) + ldsw + _i * 8192), 16, 0, 0); } while (0)
; #define PG8_LDA(dst, b, h) do { _Pragma("unroll") for (int m = 0; m < 4; ++m) _Pragma("unroll") for (int k = 0; k < 2; ++k) dst[m][k] = *(const LAS bf16x8*)(lds + PG8_SA(b, h) + ((aoff ^ (k * 64)) + m * 2048)); } while (0)
; #define PG8_MMA(ai, bj, At, Bt) do { __builtin_amdgcn_s_setprio(1); _Pragma("unroll") for (int m = 0; m < 4; ++m) _Pragma("unroll") for (int n = 0; n < 2; ++n) _Pragma("unroll") for (int k = 0; k < 2; ++k) \
;         acc[ai][bj][m][n] = __builtin_amdgcn_mfma_f32_16x16x32_bf16(Bt[n][k], At[m][k], acc[ai][bj][m][n], 0, 0, 0); __builtin_amdgcn_s_setprio(0); } while (0)
; #define PG8_WAIT_V(n) asm volatile("s_waitcnt vmcnt(" #n ")" ::: "memory")
; #define PG8_WAIT_L(n) asm volatile("s_waitcnt lgkmcnt(" #n ")" ::: "memory")
; #define PG8_BAR __builtin_amdgcn_s_barrier()
; #define PG8_SCHED __builtin_amdgcn_sched_barrier(0)
;     ...
;             PG8_LDA(At, 1, 1); PG8_STAGE(PG8_SB(1, 0), b3, voffB); PG8_STAGE(PG8_SB(1, 1), b3 + hstep, voffB); PG8_STAGE(PG8_SA(1, 0), a3, vs[0]);
;             PG8_WAIT_V(8); PG8_WAIT_L(0); PG8_BAR; if (do1) { PG8_MMA(1, 0, At, B0); PG8_MMA(1, 1, At, B1); } PG8_BAR; PG8_SCHED;
.Lld_gu1_m1b_p:
	s_barrier
	ds_read_b128 v[200:203], v161 offset:49152
	ds_read_b128 v[204:207], v161 offset:51200
	ds_read_b128 v[208:211], v162 offset:49152
	ds_read_b128 v[212:215], v162 offset:51200
	ds_read_b128 v[216:219], v161 offset:53248
	ds_read_b128 v[220:223], v161 offset:55296
	ds_read_b128 v[224:227], v162 offset:53248
	ds_read_b128 v[228:231], v162 offset:55296
	s_bitcmp1_b32 s4, 0
	s_cbranch_scc1 .Lld_gu1_sp2b_w
	s_add_i32 s2, s2, s34
	v_lshl_add_u64 v[236:237], s[24:25], 0, v[132:133]
	s_mov_b32 m0, s2
	s_nop 0
	global_load_lds_dwordx4 v[236:237], off
	s_add_i32 m0, s2, 0x2000
	s_add_u32 s2, s22, 0x44000
	v_lshl_add_u64 v[236:237], s[24:25], 0, v[134:135]
	s_addc_u32 s3, s23, 0
	s_add_i32 s22, s55, s34
	global_load_lds_dwordx4 v[236:237], off
	v_lshl_add_u64 v[236:237], s[2:3], 0, v[132:133]
	s_mov_b32 m0, s22
	v_lshl_add_u64 v[234:235], v[234:235], 0, s[10:11]
	global_load_lds_dwordx4 v[236:237], off
	v_lshl_add_u64 v[236:237], s[2:3], 0, v[134:135]
	s_add_i32 m0, s22, 0x2000
	v_lshl_add_u64 v[232:233], v[232:233], 0, s[10:11]
	global_load_lds_dwordx4 v[236:237], off
	s_mov_b32 m0, s41
	s_nop 0
	global_load_lds_dwordx4 v[234:235], off
	s_mov_b32 m0, s42
	s_nop 0
	global_load_lds_dwordx4 v[232:233], off
	s_branch .Lld_gu1_sp2b_j

; #define PG8_STAGE(bufoff, gbase, voff) do { _Pragma("unroll") for (int _i = 0; _i < 2; ++_i) \
;         __builtin_amdgcn_global_load_lds((const unsigned*)((const char*)(gbase) + (voff)[_i]), (LAS unsigned*)(lds + (bufoff) + ldsw + _i * 8192), 16, 0, 0); } while (0)
; #define PG8_LDA(dst, b, h) do { _Pragma("unroll") for (int m = 0; m < 4; ++m) _Pragma("unroll") for (int k = 0; k < 2; ++k) dst[m][k] = *(const LAS bf16x8*)(lds + PG8_SA(b, h) + ((aoff ^ (k * 64)) + m * 2048)); } while (0)
; #define PG8_MMA(ai, bj, At, Bt) do { __builtin_amdgcn_s_setprio(1); _Pragma("unroll") for (int m = 0; m < 4; ++m) _Pragma("unroll") for (int n = 0; n < 2; ++n) _Pragma("unroll") for (int k = 0; k < 2; ++k) \
;         acc[ai][bj][m][n] = __builtin_amdgcn_mfma_f32_16x16x32_bf16(Bt[n][k], At[m][k], acc[ai][bj][m][n], 0, 0, 0); __builtin_amdgcn_s_setprio(0); } while (0)
; #define PG8_WAIT_V(n) asm volatile("s_waitcnt vmcnt(" #n ")" ::: "memory")
; #define PG8_WAIT_L(n) asm volatile("s_waitcnt lgkmcnt(" #n ")" ::: "memory")
; #define PG8_BAR __builtin_amdgcn_s_barrier()
; #define PG8_SCHED __builtin_amdgcn_sched_barrier(0)
;     ...
;             PG8_LDA(At, 1, 1); PG8_STAGE(PG8_SB(1, 0), b3, voffB); PG8_STAGE(PG8_SB(1, 1), b3 + hstep, voffB); PG8_STAGE(PG8_SA(1, 0), a3, vs[0]);
;             PG8_WAIT_V(8); PG8_WAIT_L(0); PG8_BAR; if (do1) { PG8_MMA(1, 0, At, B0); PG8_MMA(1, 1, At, B1); } PG8_BAR; PG8_SCHED;
;         }
.Lld_gu1_sp2b_j:
	s_waitcnt lgkmcnt(0)
	s_barrier
	s_setprio 1
	s_waitcnt lgkmcnt(0)
	v_mfma_f32_16x16x32_bf16 v[62:65], v[166:169], v[200:203], v[62:65]
	v_mfma_f32_16x16x32_bf16 v[58:61], v[174:177], v[200:203], v[58:61]
	v_mfma_f32_16x16x32_bf16 v[46:49], v[166:169], v[204:207], v[46:49]
	v_mfma_f32_16x16x32_bf16 v[42:45], v[174:177], v[204:207], v[42:45]
	v_mfma_f32_16x16x32_bf16 v[30:33], v[166:169], v[216:219], v[30:33]
	v_mfma_f32_16x16x32_bf16 v[26:29], v[174:177], v[216:219], v[26:29]
	v_mfma_f32_16x16x32_bf16 v[14:17], v[166:169], v[220:223], v[14:17]
	v_mfma_f32_16x16x32_bf16 v[10:13], v[174:177], v[220:223], v[10:13]
	v_mfma_f32_16x16x32_bf16 v[62:65], v[170:173], v[208:211], v[62:65]
	v_mfma_f32_16x16x32_bf16 v[58:61], v[178:181], v[208:211], v[58:61]
	v_mfma_f32_16x16x32_bf16 v[46:49], v[170:173], v[212:215], v[46:49]
	v_mfma_f32_16x16x32_bf16 v[42:45], v[178:181], v[212:215], v[42:45]
	v_mfma_f32_16x16x32_bf16 v[30:33], v[170:173], v[224:227], v[30:33]
	v_mfma_f32_16x16x32_bf16 v[26:29], v[178:181], v[224:227], v[26:29]
	v_mfma_f32_16x16x32_bf16 v[14:17], v[170:173], v[228:231], v[14:17]
	v_mfma_f32_16x16x32_bf16 v[10:13], v[178:181], v[228:231], v[10:13]
	s_setprio 0
	s_setprio 1
	v_mfma_f32_16x16x32_bf16 v[54:57], v[182:185], v[200:203], v[54:57]
	v_mfma_f32_16x16x32_bf16 v[50:53], v[190:193], v[200:203], v[50:53]
	v_mfma_f32_16x16x32_bf16 v[38:41], v[182:185], v[204:207], v[38:41]
	v_mfma_f32_16x16x32_bf16 v[34:37], v[190:193], v[204:207], v[34:37]
	v_mfma_f32_16x16x32_bf16 v[22:25], v[182:185], v[216:219], v[22:25]
	v_mfma_f32_16x16x32_bf16 v[18:21], v[190:193], v[216:219], v[18:21]
	v_mfma_f32_16x16x32_bf16 v[6:9], v[182:185], v[220:223], v[6:9]
	v_mfma_f32_16x16x32_bf16 v[2:5], v[190:193], v[220:223], v[2:5]
	v_mfma_f32_16x16x32_bf16 v[54:57], v[186:189], v[208:211], v[54:57]
	v_mfma_f32_16x16x32_bf16 v[50:53], v[194:197], v[208:211], v[50:53]
	v_mfma_f32_16x16x32_bf16 v[38:41], v[186:189], v[212:215], v[38:41]
	v_mfma_f32_16x16x32_bf16 v[34:37], v[194:197], v[212:215], v[34:37]
	v_mfma_f32_16x16x32_bf16 v[22:25], v[186:189], v[224:227], v[22:25]
	v_mfma_f32_16x16x32_bf16 v[18:21], v[194:197], v[224:227], v[18:21]
	v_mfma_f32_16x16x32_bf16 v[6:9], v[186:189], v[228:231], v[6:9]
	v_mfma_f32_16x16x32_bf16 v[2:5], v[194:197], v[228:231], v[2:5]
	s_setprio 0
	s_bitcmp1_b32 s4, 0
	s_cbranch_scc1 .Lld_gu1_m2b_p
	s_waitcnt vmcnt(8)
.Lld_gu1_m2b_p:
	s_barrier
	s_add_i32 s54, s54, 2
	s_add_u32 s13, s13, 0x8000
	s_addc_u32 s53, s53, 0
	s_add_u32 s20, s20, 0x100
	s_addc_u32 s21, s21, 0
	s_cmp_gt_u32 s54, 13
	s_cbranch_scc1 .LBB0_2340
